# HID stores of the SwiGLU epilogue marked nt (write once, read from HBM later)
# baseline (speedup 1.0000x reference)
; template <bool BF> __device__ __forceinline__ unsigned pk16(float lo, float hi) { return BF ? pkb(lo, hi) : pkh(lo, hi); }
;     __device__ __forceinline__ void operator()(const Acc& acc, const Unit& u, int wr, int wc, int fr, int fq) const {
;         const int row0 = u.pm * BM + wr * 64 + fr, col0 = u.pn * HALF + wc * 32 + 8 * fq;
;         f16* Og = O + (size_t)u.g * EROWS * DE;
; #pragma unroll
;         for (int ai = 0; ai < 2; ++ai)
; #pragma unroll
;             for (int m = 0; m < 4; ++m) { f16* rowp = Og + (size_t)(row0 + ai * HALF + m * 16) * DE + col0;
;                 float h[8];
; #pragma unroll
;                 for (int n = 0; n < 2; ++n)
; #pragma unroll
;                     for (int j = 0; j < 4; ++j) { const float g = acc[ai][0][m][n][j], up = acc[ai][1][m][n][j]; h[n * 4 + j] = g * up * __builtin_amdgcn_rcpf(1.f + __builtin_amdgcn_exp2f(-LOG2E * g)); }
;                 u32x4 w; w.x = pk16<MOE_BF16>(h[0], h[1]); w.y = pk16<MOE_BF16>(h[2], h[3]); w.z = pk16<MOE_BF16>(h[4], h[5]); w.w = pk16<MOE_BF16>(h[6], h[7]);
;                 *(u32x4*)rowp = w; }
.LBB0_1014:
	v_mul_f32_e32 v141, 0xbfb8aa3b, v98
	v_exp_f32_e32 v141, v141
	v_mul_f32_e32 v145, 0xbfb8aa3b, v99
	v_exp_f32_e32 v145, v145
	v_pk_mul_f32 v[166:167], v[98:99], v[66:67]
	v_add_f32_e32 v141, 1.0, v141
	v_rcp_f32_e32 v150, v141
	v_add_f32_e32 v141, 1.0, v145
	v_rcp_f32_e32 v151, v141
	v_mul_f32_e32 v141, 0xbfb8aa3b, v100
	v_exp_f32_e32 v141, v141
	v_mul_f32_e32 v145, 0xbfb8aa3b, v101
	v_exp_f32_e32 v145, v145
	v_pk_mul_f32 v[150:151], v[150:151], v[166:167]
	v_add_f32_e32 v141, 1.0, v141
	v_rcp_f32_e32 v166, v141
	v_add_f32_e32 v141, 1.0, v145
	v_rcp_f32_e32 v167, v141
	v_mul_f32_e32 v141, 0xbfb8aa3b, v94
	v_exp_f32_e32 v141, v141
	v_mul_f32_e32 v145, 0xbfb8aa3b, v95
	v_exp_f32_e32 v145, v145
	v_pk_mul_f32 v[164:165], v[100:101], v[68:69]
	v_add_f32_e32 v141, 1.0, v141
	v_pk_mul_f32 v[166:167], v[166:167], v[164:165]
	v_rcp_f32_e32 v164, v141
	v_add_f32_e32 v141, 1.0, v145
	v_mul_f32_e32 v145, 0xbfb8aa3b, v96
	v_exp_f32_e32 v145, v145
	v_mul_f32_e32 v163, 0xbfb8aa3b, v97
	v_exp_f32_e32 v163, v163
	v_rcp_f32_e32 v165, v141
	v_add_f32_e32 v141, 1.0, v145
	v_rcp_f32_e32 v168, v141
	v_add_f32_e32 v141, 1.0, v163
	v_rcp_f32_e32 v169, v141
	v_mul_f32_e32 v141, 0xbfb8aa3b, v90
	v_exp_f32_e32 v141, v141
	v_mul_f32_e32 v145, 0xbfb8aa3b, v91
	v_exp_f32_e32 v145, v145
	v_pk_mul_f32 v[172:173], v[94:95], v[62:63]
	v_add_f32_e32 v141, 1.0, v141
	s_add_u32 s2, s21, 0xffffff00
	v_pk_mul_f32 v[172:173], v[164:165], v[172:173]
	v_cvt_pk_bf16_f32 v164, v150, v151
	v_rcp_f32_e32 v150, v141
	v_add_f32_e32 v141, 1.0, v145
	s_addc_u32 s3, s42, -1
	s_mul_i32 s22, s26, 0x1600000
	v_rcp_f32_e32 v151, v141
	v_mul_f32_e32 v141, 0xbfb8aa3b, v92
	v_lshl_or_b32 v148, s10, 7, v143
	s_mul_hi_i32 s21, s26, 0x1600000
	s_add_u32 s22, s76, s22
	v_exp_f32_e32 v141, v141
	v_mul_f32_e32 v145, 0xbfb8aa3b, v93
	s_addc_u32 s23, s77, s21
	v_ashrrev_i32_e32 v149, 31, v148
	v_pk_mul_f32 v[170:171], v[96:97], v[64:65]
	v_exp_f32_e32 v145, v145
	v_lshl_add_u32 v134, s27, 8, v155
	v_lshl_add_u64 v[148:149], v[148:149], 1, s[22:23]
	v_pk_mul_f32 v[168:169], v[168:169], v[170:171]
	v_mad_i64_i32 v[170:171], s[22:23], v134, s37, v[148:149]
	v_cvt_pk_bf16_f32 v165, v166, v167
	v_cvt_pk_bf16_f32 v166, v172, v173
	v_cvt_pk_bf16_f32 v167, v168, v169
	global_store_dwordx4 v[170:171], v[164:167], off nt
	v_add_f32_e32 v141, 1.0, v141
	v_pk_mul_f32 v[172:173], v[86:87], v[54:55]
	v_pk_mul_f32 v[166:167], v[90:91], v[58:59]
	v_pk_mul_f32 v[164:165], v[92:93], v[60:61]
	v_pk_mul_f32 v[150:151], v[150:151], v[166:167]
	v_rcp_f32_e32 v166, v141
	v_add_f32_e32 v141, 1.0, v145
	v_rcp_f32_e32 v167, v141
	v_mul_f32_e32 v141, 0xbfb8aa3b, v86
	v_exp_f32_e32 v141, v141
	v_mul_f32_e32 v145, 0xbfb8aa3b, v87
	v_exp_f32_e32 v145, v145
	v_pk_mul_f32 v[166:167], v[166:167], v[164:165]
	v_add_f32_e32 v141, 1.0, v141
	v_rcp_f32_e32 v164, v141
	v_add_f32_e32 v141, 1.0, v145
	v_mul_f32_e32 v145, 0xbfb8aa3b, v88
	v_exp_f32_e32 v145, v145
	v_mul_f32_e32 v165, 0xbfb8aa3b, v89
	v_exp_f32_e32 v169, v165
	v_rcp_f32_e32 v165, v141
	v_add_f32_e32 v141, 1.0, v145
	v_rcp_f32_e32 v168, v141
	v_add_f32_e32 v141, 1.0, v169
	v_rcp_f32_e32 v169, v141
	v_mul_f32_e32 v141, 0xbfb8aa3b, v82
	v_exp_f32_e32 v141, v141
	v_mul_f32_e32 v145, 0xbfb8aa3b, v83
	v_exp_f32_e32 v145, v145
	v_pk_mul_f32 v[172:173], v[164:165], v[172:173]
	v_add_f32_e32 v141, 1.0, v141
	v_cvt_pk_bf16_f32 v164, v150, v151
	v_rcp_f32_e32 v150, v141
	v_add_f32_e32 v141, 1.0, v145
	v_rcp_f32_e32 v151, v141
	v_mul_f32_e32 v141, 0xbfb8aa3b, v84
	v_exp_f32_e32 v141, v141
	v_mul_f32_e32 v145, 0xbfb8aa3b, v85
	v_pk_mul_f32 v[170:171], v[88:89], v[56:57]
	v_exp_f32_e32 v145, v145
	v_or_b32_e32 v163, 16, v134
	v_pk_mul_f32 v[168:169], v[168:169], v[170:171]
	v_mad_i64_i32 v[170:171], s[22:23], v163, s37, v[148:149]
	v_cvt_pk_bf16_f32 v165, v166, v167
	v_cvt_pk_bf16_f32 v166, v172, v173
	v_cvt_pk_bf16_f32 v167, v168, v169
	global_store_dwordx4 v[170:171], v[164:167], off nt
	v_add_f32_e32 v141, 1.0, v141
	v_pk_mul_f32 v[172:173], v[78:79], v[46:47]
	v_pk_mul_f32 v[166:167], v[82:83], v[50:51]
	v_pk_mul_f32 v[164:165], v[84:85], v[52:53]
	v_pk_mul_f32 v[150:151], v[150:151], v[166:167]
	v_rcp_f32_e32 v166, v141
	v_add_f32_e32 v141, 1.0, v145
	v_rcp_f32_e32 v167, v141
	v_mul_f32_e32 v141, 0xbfb8aa3b, v78
	v_exp_f32_e32 v141, v141
	v_mul_f32_e32 v145, 0xbfb8aa3b, v79
	v_exp_f32_e32 v145, v145
	v_pk_mul_f32 v[166:167], v[166:167], v[164:165]
	v_add_f32_e32 v141, 1.0, v141
	v_rcp_f32_e32 v164, v141
	v_add_f32_e32 v141, 1.0, v145
	v_mul_f32_e32 v145, 0xbfb8aa3b, v80
	v_exp_f32_e32 v145, v145
	v_mul_f32_e32 v165, 0xbfb8aa3b, v81
	v_exp_f32_e32 v169, v165
	v_rcp_f32_e32 v165, v141
	v_add_f32_e32 v141, 1.0, v145
	v_rcp_f32_e32 v168, v141
	v_add_f32_e32 v141, 1.0, v169
	v_rcp_f32_e32 v169, v141
	v_mul_f32_e32 v141, 0xbfb8aa3b, v74
	v_exp_f32_e32 v141, v141
	v_mul_f32_e32 v145, 0xbfb8aa3b, v75
	v_exp_f32_e32 v145, v145
	v_pk_mul_f32 v[172:173], v[164:165], v[172:173]
	v_add_f32_e32 v141, 1.0, v141
	v_cvt_pk_bf16_f32 v164, v150, v151
	v_rcp_f32_e32 v150, v141
	v_add_f32_e32 v141, 1.0, v145
	v_rcp_f32_e32 v151, v141
	v_mul_f32_e32 v141, 0xbfb8aa3b, v76
	v_exp_f32_e32 v141, v141
	v_mul_f32_e32 v145, 0xbfb8aa3b, v77
	v_pk_mul_f32 v[170:171], v[80:81], v[48:49]
	v_exp_f32_e32 v145, v145
	v_or_b32_e32 v163, 32, v134
	v_pk_mul_f32 v[168:169], v[168:169], v[170:171]
	v_mad_i64_i32 v[170:171], s[22:23], v163, s37, v[148:149]
	v_cvt_pk_bf16_f32 v165, v166, v167
	v_cvt_pk_bf16_f32 v166, v172, v173
	v_cvt_pk_bf16_f32 v167, v168, v169
	global_store_dwordx4 v[170:171], v[164:167], off nt
	v_add_f32_e32 v141, 1.0, v141
	v_pk_mul_f32 v[172:173], v[70:71], v[38:39]
; template <bool BF> __device__ __forceinline__ unsigned pk16(float lo, float hi) { return BF ? pkb(lo, hi) : pkh(lo, hi); }
;     __device__ __forceinline__ void operator()(const Acc& acc, const Unit& u, int wr, int wc, int fr, int fq) const {
;     ...
;             for (int m = 0; m < 4; ++m) { f16* rowp = Og + (size_t)(row0 + ai * HALF + m * 16) * DE + col0;
;                 float h[8];
; #pragma unroll
;                 for (int n = 0; n < 2; ++n)
; #pragma unroll
;                     for (int j = 0; j < 4; ++j) { const float g = acc[ai][0][m][n][j], up = acc[ai][1][m][n][j]; h[n * 4 + j] = g * up * __builtin_amdgcn_rcpf(1.f + __builtin_amdgcn_exp2f(-LOG2E * g)); }
;                 u32x4 w; w.x = pk16<MOE_BF16>(h[0], h[1]); w.y = pk16<MOE_BF16>(h[2], h[3]); w.z = pk16<MOE_BF16>(h[4], h[5]); w.w = pk16<MOE_BF16>(h[6], h[7]);
;                 *(u32x4*)rowp = w; }
	v_pk_mul_f32 v[166:167], v[74:75], v[42:43]
	v_pk_mul_f32 v[164:165], v[76:77], v[44:45]
	v_pk_mul_f32 v[150:151], v[150:151], v[166:167]
	v_rcp_f32_e32 v166, v141
	v_add_f32_e32 v141, 1.0, v145
	v_rcp_f32_e32 v167, v141
	v_mul_f32_e32 v141, 0xbfb8aa3b, v70
	v_exp_f32_e32 v141, v141
	v_mul_f32_e32 v145, 0xbfb8aa3b, v71
	v_exp_f32_e32 v145, v145
	v_pk_mul_f32 v[166:167], v[166:167], v[164:165]
	v_add_f32_e32 v141, 1.0, v141
	v_rcp_f32_e32 v164, v141
	v_add_f32_e32 v141, 1.0, v145
	v_mul_f32_e32 v145, 0xbfb8aa3b, v72
	v_exp_f32_e32 v145, v145
	v_mul_f32_e32 v165, 0xbfb8aa3b, v73
	v_exp_f32_e32 v169, v165
	v_rcp_f32_e32 v165, v141
	v_add_f32_e32 v141, 1.0, v145
	v_rcp_f32_e32 v168, v141
	v_add_f32_e32 v141, 1.0, v169
	v_rcp_f32_e32 v169, v141
	v_mul_f32_e32 v141, 0xbfb8aa3b, v34
	v_exp_f32_e32 v141, v141
	v_mul_f32_e32 v145, 0xbfb8aa3b, v35
	v_exp_f32_e32 v145, v145
	v_pk_mul_f32 v[172:173], v[164:165], v[172:173]
	v_add_f32_e32 v141, 1.0, v141
	v_cvt_pk_bf16_f32 v164, v150, v151
	v_rcp_f32_e32 v150, v141
	v_add_f32_e32 v141, 1.0, v145
	v_rcp_f32_e32 v151, v141
	v_mul_f32_e32 v141, 0xbfb8aa3b, v36
	v_exp_f32_e32 v141, v141
	v_mul_f32_e32 v145, 0xbfb8aa3b, v37
	v_pk_mul_f32 v[170:171], v[72:73], v[40:41]
	v_exp_f32_e32 v145, v145
	v_or_b32_e32 v163, 48, v134
	v_pk_mul_f32 v[168:169], v[168:169], v[170:171]
	v_mad_i64_i32 v[170:171], s[22:23], v163, s37, v[148:149]
	v_cvt_pk_bf16_f32 v165, v166, v167
	v_cvt_pk_bf16_f32 v166, v172, v173
	v_cvt_pk_bf16_f32 v167, v168, v169
	global_store_dwordx4 v[170:171], v[164:167], off nt
	v_add_f32_e32 v141, 1.0, v141
	v_pk_mul_f32 v[172:173], v[30:31], v[102:103]
	v_pk_mul_f32 v[166:167], v[34:35], v[2:3]
	v_pk_mul_f32 v[164:165], v[36:37], v[4:5]
	v_pk_mul_f32 v[150:151], v[150:151], v[166:167]
	v_rcp_f32_e32 v166, v141
	v_add_f32_e32 v141, 1.0, v145
	v_rcp_f32_e32 v167, v141
	v_mul_f32_e32 v141, 0xbfb8aa3b, v30
	v_exp_f32_e32 v141, v141
	v_mul_f32_e32 v145, 0xbfb8aa3b, v31
	v_exp_f32_e32 v145, v145
	v_pk_mul_f32 v[166:167], v[166:167], v[164:165]
	v_add_f32_e32 v141, 1.0, v141
	v_rcp_f32_e32 v164, v141
	v_add_f32_e32 v141, 1.0, v145
	v_mul_f32_e32 v145, 0xbfb8aa3b, v32
	v_exp_f32_e32 v145, v145
	v_mul_f32_e32 v165, 0xbfb8aa3b, v33
	v_exp_f32_e32 v169, v165
	v_rcp_f32_e32 v165, v141
	v_add_f32_e32 v141, 1.0, v145
	v_rcp_f32_e32 v168, v141
	v_add_f32_e32 v141, 1.0, v169
	v_rcp_f32_e32 v169, v141
	v_mul_f32_e32 v141, 0xbfb8aa3b, v26
	v_exp_f32_e32 v141, v141
	v_mul_f32_e32 v145, 0xbfb8aa3b, v27
	v_exp_f32_e32 v145, v145
	v_pk_mul_f32 v[172:173], v[164:165], v[172:173]
	v_add_f32_e32 v141, 1.0, v141
	v_cvt_pk_bf16_f32 v164, v150, v151
	v_rcp_f32_e32 v150, v141
	v_add_f32_e32 v141, 1.0, v145
	v_rcp_f32_e32 v151, v141
	v_mul_f32_e32 v141, 0xbfb8aa3b, v28
	v_exp_f32_e32 v141, v141
	v_mul_f32_e32 v145, 0xbfb8aa3b, v29
	v_pk_mul_f32 v[170:171], v[32:33], v[104:105]
	v_exp_f32_e32 v145, v145
	v_add_u32_e32 v163, 0x80, v134
	v_pk_mul_f32 v[168:169], v[168:169], v[170:171]
	v_mad_i64_i32 v[170:171], s[22:23], v163, s37, v[148:149]
	v_cvt_pk_bf16_f32 v165, v166, v167
	v_cvt_pk_bf16_f32 v166, v172, v173
	v_cvt_pk_bf16_f32 v167, v168, v169
	global_store_dwordx4 v[170:171], v[164:167], off nt
	v_add_f32_e32 v141, 1.0, v141
	v_pk_mul_f32 v[172:173], v[22:23], v[110:111]
	v_pk_mul_f32 v[166:167], v[26:27], v[106:107]
	v_pk_mul_f32 v[164:165], v[28:29], v[108:109]
	v_pk_mul_f32 v[150:151], v[150:151], v[166:167]
	v_rcp_f32_e32 v166, v141
	v_add_f32_e32 v141, 1.0, v145
	v_rcp_f32_e32 v167, v141
	v_mul_f32_e32 v141, 0xbfb8aa3b, v22
	v_exp_f32_e32 v141, v141
	v_mul_f32_e32 v145, 0xbfb8aa3b, v23
	v_exp_f32_e32 v145, v145
	v_pk_mul_f32 v[166:167], v[166:167], v[164:165]
	v_add_f32_e32 v141, 1.0, v141
	v_rcp_f32_e32 v164, v141
	v_add_f32_e32 v141, 1.0, v145
	v_mul_f32_e32 v145, 0xbfb8aa3b, v24
	v_exp_f32_e32 v145, v145
	v_mul_f32_e32 v165, 0xbfb8aa3b, v25
	v_exp_f32_e32 v169, v165
	v_rcp_f32_e32 v165, v141
	v_add_f32_e32 v141, 1.0, v145
; template <bool BF> __device__ __forceinline__ unsigned pk16(float lo, float hi) { return BF ? pkb(lo, hi) : pkh(lo, hi); }
; #define GM_BAR __builtin_amdgcn_s_barrier()
;     __device__ __forceinline__ void operator()(const Acc& acc, const Unit& u, int wr, int wc, int fr, int fq) const {
;     ...
;             for (int m = 0; m < 4; ++m) { f16* rowp = Og + (size_t)(row0 + ai * HALF + m * 16) * DE + col0;
;                 float h[8];
; #pragma unroll
;                 for (int n = 0; n < 2; ++n)
; #pragma unroll
;                     for (int j = 0; j < 4; ++j) { const float g = acc[ai][0][m][n][j], up = acc[ai][1][m][n][j]; h[n * 4 + j] = g * up * __builtin_amdgcn_rcpf(1.f + __builtin_amdgcn_exp2f(-LOG2E * g)); }
;                 u32x4 w; w.x = pk16<MOE_BF16>(h[0], h[1]); w.y = pk16<MOE_BF16>(h[2], h[3]); w.z = pk16<MOE_BF16>(h[4], h[5]); w.w = pk16<MOE_BF16>(h[6], h[7]);
;                 *(u32x4*)rowp = w; }
; template <bool BF, bool GATHER = false, class Epi, class Hook>
; __device__ __forceinline__ void gemm_phase(LAS unsigned char* lds, const Gemm g, const Order& S, const Epi& E, Hook& HK) {
;     ...
;         if (!has_next) break;
; #pragma unroll
;         for (int a = 0; a < 2; ++a)
; #pragma unroll
;             for (int b = 0; b < 2; ++b)
; #pragma unroll
;                 for (int m = 0; m < 4; ++m)
; #pragma unroll
;                     for (int n = 0; n < 2; ++n) acc[a][b][m][n] = (f32x4){0.f, 0.f, 0.f, 0.f};
;         cur = nxt; cA = nA; cB = nB; ++ui;
;         if constexpr (GATHER) { gA0[0] = nA0[0]; gA0[1] = nA0[1]; gA1[0] = nA1[0]; gA1[1] = nA1[1]; }
;         if (wr == 1) GM_BAR;
	v_rcp_f32_e32 v168, v141
	v_add_f32_e32 v141, 1.0, v169
	v_rcp_f32_e32 v169, v141
	v_mul_f32_e32 v141, 0xbfb8aa3b, v18
	v_exp_f32_e32 v141, v141
	v_mul_f32_e32 v145, 0xbfb8aa3b, v19
	v_exp_f32_e32 v145, v145
	v_pk_mul_f32 v[172:173], v[164:165], v[172:173]
	v_add_f32_e32 v141, 1.0, v141
	v_cvt_pk_bf16_f32 v164, v150, v151
	v_rcp_f32_e32 v150, v141
	v_add_f32_e32 v141, 1.0, v145
	v_rcp_f32_e32 v151, v141
	v_mul_f32_e32 v141, 0xbfb8aa3b, v20
	v_exp_f32_e32 v141, v141
	v_mul_f32_e32 v145, 0xbfb8aa3b, v21
	v_pk_mul_f32 v[170:171], v[24:25], v[112:113]
	v_exp_f32_e32 v145, v145
	v_add_u32_e32 v163, 0x90, v134
	v_pk_mul_f32 v[168:169], v[168:169], v[170:171]
	v_mad_i64_i32 v[170:171], s[22:23], v163, s37, v[148:149]
	v_cvt_pk_bf16_f32 v165, v166, v167
	v_cvt_pk_bf16_f32 v166, v172, v173
	v_cvt_pk_bf16_f32 v167, v168, v169
	global_store_dwordx4 v[170:171], v[164:167], off nt
	v_add_f32_e32 v141, 1.0, v141
	v_pk_mul_f32 v[172:173], v[14:15], v[118:119]
	v_pk_mul_f32 v[166:167], v[18:19], v[114:115]
	v_pk_mul_f32 v[164:165], v[20:21], v[116:117]
	v_pk_mul_f32 v[150:151], v[150:151], v[166:167]
	v_rcp_f32_e32 v166, v141
	v_add_f32_e32 v141, 1.0, v145
	v_rcp_f32_e32 v167, v141
	v_mul_f32_e32 v141, 0xbfb8aa3b, v14
	v_exp_f32_e32 v141, v141
	v_mul_f32_e32 v145, 0xbfb8aa3b, v15
	v_exp_f32_e32 v145, v145
	v_pk_mul_f32 v[166:167], v[166:167], v[164:165]
	v_add_f32_e32 v141, 1.0, v141
	v_rcp_f32_e32 v164, v141
	v_add_f32_e32 v141, 1.0, v145
	v_mul_f32_e32 v145, 0xbfb8aa3b, v16
	v_exp_f32_e32 v145, v145
	v_mul_f32_e32 v165, 0xbfb8aa3b, v17
	v_exp_f32_e32 v169, v165
	v_rcp_f32_e32 v165, v141
	v_add_f32_e32 v141, 1.0, v145
	v_rcp_f32_e32 v168, v141
	v_add_f32_e32 v141, 1.0, v169
	v_rcp_f32_e32 v169, v141
	v_mul_f32_e32 v141, 0xbfb8aa3b, v10
	v_exp_f32_e32 v141, v141
	v_mul_f32_e32 v145, 0xbfb8aa3b, v11
	v_exp_f32_e32 v145, v145
	v_pk_mul_f32 v[172:173], v[164:165], v[172:173]
	v_add_f32_e32 v141, 1.0, v141
	v_cvt_pk_bf16_f32 v164, v150, v151
	v_rcp_f32_e32 v150, v141
	v_add_f32_e32 v141, 1.0, v145
	v_rcp_f32_e32 v151, v141
	v_mul_f32_e32 v141, 0xbfb8aa3b, v12
	v_exp_f32_e32 v141, v141
	v_mul_f32_e32 v145, 0xbfb8aa3b, v13
	v_pk_mul_f32 v[170:171], v[16:17], v[120:121]
	v_exp_f32_e32 v145, v145
	v_add_u32_e32 v163, 0xa0, v134
	v_pk_mul_f32 v[168:169], v[168:169], v[170:171]
	v_mad_i64_i32 v[170:171], s[22:23], v163, s37, v[148:149]
	v_cvt_pk_bf16_f32 v165, v166, v167
	v_cvt_pk_bf16_f32 v166, v172, v173
	v_cvt_pk_bf16_f32 v167, v168, v169
	global_store_dwordx4 v[170:171], v[164:167], off nt
	v_add_f32_e32 v141, 1.0, v141
	v_mul_f32_e32 v163, 0xbfb8aa3b, v9
	v_pk_mul_f32 v[166:167], v[10:11], v[122:123]
	v_pk_mul_f32 v[164:165], v[12:13], v[124:125]
	v_pk_mul_f32 v[150:151], v[150:151], v[166:167]
	v_rcp_f32_e32 v166, v141
	v_add_f32_e32 v141, 1.0, v145
	v_rcp_f32_e32 v167, v141
	v_mul_f32_e32 v141, 0xbfb8aa3b, v6
	v_exp_f32_e32 v141, v141
	v_mul_f32_e32 v145, 0xbfb8aa3b, v7
	v_exp_f32_e32 v145, v145
	v_pk_mul_f32 v[164:165], v[166:167], v[164:165]
	v_add_f32_e32 v141, 1.0, v141
	v_rcp_f32_e32 v166, v141
	v_add_f32_e32 v141, 1.0, v145
	v_mul_f32_e32 v145, 0xbfb8aa3b, v8
	v_exp_f32_e32 v145, v145
	v_exp_f32_e32 v163, v163
	v_rcp_f32_e32 v167, v141
	v_pk_mul_f32 v[170:171], v[8:9], v[128:129]
	v_add_f32_e32 v141, 1.0, v145
	v_rcp_f32_e32 v168, v141
	v_add_f32_e32 v141, 1.0, v163
	v_rcp_f32_e32 v169, v141
	v_pk_mul_f32 v[172:173], v[6:7], v[126:127]
	v_add_u32_e32 v134, 0xb0, v134
	v_pk_mul_f32 v[166:167], v[166:167], v[172:173]
	v_pk_mul_f32 v[168:169], v[168:169], v[170:171]
	v_mad_i64_i32 v[170:171], s[22:23], v134, s37, v[148:149]
	v_cvt_pk_bf16_f32 v148, v150, v151
	v_cvt_pk_bf16_f32 v149, v164, v165
	v_cvt_pk_bf16_f32 v150, v166, v167
	v_cvt_pk_bf16_f32 v151, v168, v169
	s_and_b64 vcc, exec, s[6:7]
	global_store_dwordx4 v[170:171], v[148:151], off nt
	s_cbranch_vccnz .LBB0_1017
	s_andn2_b64 vcc, exec, s[12:13]
	s_cbranch_vccnz .LBB0_1003
	s_barrier
	s_branch .LBB0_1003
